# nt on read-once activation loads: x in phase 1 and in the out-proj epilogue, residual/expert rows in the combine phase
# speedup vs baseline: 1.0116x; 1.0116x over previous
; #define LAS __attribute__((address_space(3)))
; template <int R, bool RT = false>
; __device__ __forceinline__ void norm_phase(const NormArgs& a, LAS unsigned char* lds, bool ctx_rows, const float* ctx_src, const float* ctx_shift, const float* ctx_scale) {
;     ...
;             for (int q = 0; q < R; ++q) { const int row = row0 + rr + q;
;                 if (a.src16) { const f16* xr = a.src16 + (size_t)row * DM;
; #pragma unroll
;                     for (int j = 0; j < 4; ++j) { const f16x4 t = *(const f16x4*)(xr + 4 * lane + 256 * j); v[q][j] = (f32x4){(float)t[0], (float)t[1], (float)t[2], (float)t[3]};
;                         if constexpr (RT) { if (j == 0) *(LAS u32x2*)(hs + (rr + q) * 528 + 8 * lane) = __builtin_bit_cast(u32x2, t);
;                             else xp[rr / 4][q][j - 1] = __builtin_bit_cast(u32x2, t); } } }
;                 else { const float* xr = a.src + (size_t)row * DM;
; #pragma unroll
;                     for (int j = 0; j < 4; ++j) v[q][j] = *(const f32x4*)(xr + 4 * lane + 256 * j); } }
;     ...
;             for (int q = 0; q < R; ++q) { float ss = 0.f;
; #pragma unroll
;                 for (int j = 0; j < 4; ++j) ss += (v[q][j][0] * v[q][j][0] + v[q][j][1] * v[q][j][1]) + (v[q][j][2] * v[q][j][2] + v[q][j][3] * v[q][j][3]);
;                 rstd[q] = __builtin_amdgcn_rsqf(wave_sum(ss) * (1.f / DM) + EPS);
.LBB0_308:
	v_lshl_add_u64 v[18:19], s[16:17], 0, v[30:31]
	v_lshl_add_u64 v[20:21], s[22:23], 0, v[30:31]
	v_lshl_add_u64 v[48:49], s[28:29], 0, v[30:31]
	v_lshl_add_u64 v[50:51], s[20:21], 0, v[30:31]
	global_load_dwordx4 v[68:71], v[18:19], off nt
	global_load_dwordx4 v[72:75], v[18:19], off offset:1024 nt
	global_load_dwordx4 v[76:79], v[18:19], off offset:3072 nt
	global_load_dwordx4 v[80:83], v[18:19], off offset:2048 nt
	global_load_dwordx4 v[84:87], v[20:21], off nt
	global_load_dwordx4 v[88:91], v[20:21], off offset:1024 nt
	global_load_dwordx4 v[92:95], v[20:21], off offset:3072 nt
	global_load_dwordx4 v[96:99], v[20:21], off offset:2048 nt
	global_load_dwordx4 v[100:103], v[48:49], off nt
	global_load_dwordx4 v[104:107], v[48:49], off offset:1024 nt
	global_load_dwordx4 v[108:111], v[48:49], off offset:3072 nt
	global_load_dwordx4 v[112:115], v[48:49], off offset:2048 nt
	global_load_dwordx4 v[116:119], v[50:51], off nt
	global_load_dwordx4 v[120:123], v[50:51], off offset:1024 nt
	global_load_dwordx4 v[18:21], v[50:51], off offset:3072 nt
	global_load_dwordx4 v[124:127], v[50:51], off offset:2048 nt
	v_lshl_add_u64 v[52:53], s[14:15], 0, v[22:23]
	v_add_co_u32_e32 v54, vcc, s7, v52
	v_lshl_add_u64 v[128:129], s[18:19], 0, v[22:23]
	s_nop 0
	v_addc_co_u32_e32 v55, vcc, 0, v53, vcc
	v_add_co_u32_e32 v52, vcc, s7, v128
	v_lshl_add_u64 v[130:131], s[24:25], 0, v[22:23]
	s_nop 0
	v_addc_co_u32_e32 v53, vcc, 0, v129, vcc
	v_add_co_u32_e32 v50, vcc, s7, v130
	v_lshl_add_u64 v[132:133], s[26:27], 0, v[22:23]
	s_nop 0
	v_addc_co_u32_e32 v51, vcc, 0, v131, vcc
	v_add_co_u32_e32 v48, vcc, s7, v132
	s_add_u32 s14, s14, 0x2000
	s_nop 0
	v_addc_co_u32_e32 v49, vcc, 0, v133, vcc
	s_addc_u32 s15, s15, 0
	s_add_i32 s3, s3, 4
	s_add_u32 s16, s16, 0x4000
	v_mov_b32_e32 v61, 0
	s_addc_u32 s17, s17, 0
	v_mov_b32_e32 v63, 0
	v_mov_b32_e32 v65, 0
	v_mov_b32_e32 v67, 0
	s_add_u32 s18, s18, 0x2000
	v_mov_b32_e32 v60, 0
	s_addc_u32 s19, s19, 0
	v_mov_b32_e32 v62, 0
	v_mov_b32_e32 v64, 0
	v_mov_b32_e32 v66, 0
	s_add_u32 s20, s20, 0x4000
	s_addc_u32 s21, s21, 0
	s_add_u32 s22, s22, 0x4000
	s_addc_u32 s23, s23, 0
	s_add_u32 s24, s24, 0x2000
	s_addc_u32 s25, s25, 0
	s_add_u32 s26, s26, 0x2000
	s_addc_u32 s27, s27, 0
	s_add_u32 s28, s28, 0x4000
	s_addc_u32 s29, s29, 0
	s_cmp_gt_u32 s3, 11
	s_waitcnt vmcnt(15)
	v_pk_mul_f32 v[128:129], v[70:71], v[70:71]
	v_pk_mul_f32 v[130:131], v[68:69], v[68:69]
	s_waitcnt vmcnt(14)
	v_pk_mul_f32 v[132:133], v[74:75], v[74:75]
	v_pk_mul_f32 v[134:135], v[72:73], v[72:73]
	s_waitcnt vmcnt(12)
	v_mul_f32_e32 v136, v81, v81
	v_mul_f32_e32 v138, v83, v83
	s_waitcnt vmcnt(11)
	v_pk_mul_f32 v[140:141], v[86:87], v[86:87]
	v_pk_mul_f32 v[142:143], v[84:85], v[84:85]
	s_waitcnt vmcnt(10)
	v_pk_mul_f32 v[144:145], v[90:91], v[90:91]
	v_pk_mul_f32 v[146:147], v[88:89], v[88:89]
	s_waitcnt vmcnt(8)
	v_mul_f32_e32 v148, v97, v97
	v_mul_f32_e32 v150, v99, v99
	s_waitcnt vmcnt(7)
	v_pk_mul_f32 v[152:153], v[102:103], v[102:103]
	v_pk_mul_f32 v[154:155], v[100:101], v[100:101]
	s_waitcnt vmcnt(6)
	v_pk_mul_f32 v[156:157], v[106:107], v[106:107]
	v_pk_mul_f32 v[158:159], v[104:105], v[104:105]
	s_waitcnt vmcnt(4)
	v_mul_f32_e32 v160, v113, v113
	v_mul_f32_e32 v162, v115, v115
	s_waitcnt vmcnt(3)
	v_pk_mul_f32 v[164:165], v[118:119], v[118:119]
	v_pk_mul_f32 v[166:167], v[116:117], v[116:117]
	s_waitcnt vmcnt(2)
	v_pk_mul_f32 v[168:169], v[122:123], v[122:123]
	v_pk_mul_f32 v[170:171], v[120:121], v[120:121]
	v_pk_mov_b32 v[176:177], v[130:131], v[128:129] op_sel:[1,0]
	v_mov_b32_e32 v131, v129
	v_pk_mov_b32 v[128:129], v[134:135], v[132:133] op_sel:[1,0]
	v_mov_b32_e32 v135, v133
	v_mul_f32_e32 v179, v78, v78
	v_mul_f32_e32 v180, v79, v79
	v_mul_f32_e32 v183, v94, v94
	v_mul_f32_e32 v184, v95, v95
	v_pk_fma_f32 v[132:133], v[80:81], v[80:81], v[136:137] op_sel_hi:[1,1,0]
	v_pk_fma_f32 v[136:137], v[82:83], v[82:83], v[138:139] op_sel_hi:[1,1,0]
	v_pk_mov_b32 v[138:139], v[142:143], v[140:141] op_sel:[1,0]
	v_mov_b32_e32 v143, v141
	v_pk_mov_b32 v[140:141], v[146:147], v[144:145] op_sel:[1,0]
	v_mov_b32_e32 v147, v145
	v_pk_fma_f32 v[144:145], v[96:97], v[96:97], v[148:149] op_sel_hi:[1,1,0]
	v_pk_fma_f32 v[148:149], v[98:99], v[98:99], v[150:151] op_sel_hi:[1,1,0]
	v_pk_mov_b32 v[150:151], v[154:155], v[152:153] op_sel:[1,0]
	v_mov_b32_e32 v155, v153
	v_pk_mov_b32 v[152:153], v[158:159], v[156:157] op_sel:[1,0]
	v_mov_b32_e32 v159, v157
	v_pk_fma_f32 v[156:157], v[112:113], v[112:113], v[160:161] op_sel_hi:[1,1,0]
	v_pk_fma_f32 v[160:161], v[114:115], v[114:115], v[162:163] op_sel_hi:[1,1,0]
	v_pk_mov_b32 v[162:163], v[166:167], v[164:165] op_sel:[1,0]
	v_mov_b32_e32 v167, v165
	v_pk_mov_b32 v[164:165], v[170:171], v[168:169] op_sel:[1,0]
	v_mov_b32_e32 v171, v169
	v_pk_add_f32 v[130:131], v[176:177], v[130:131]
	v_pk_add_f32 v[128:129], v[128:129], v[134:135]
	v_mul_f32_e32 v175, v76, v76
	v_mul_f32_e32 v178, v77, v77
	s_waitcnt vmcnt(0)
; #define WS_DPP(x, ctrl, rmask) __builtin_bit_cast(float, __builtin_amdgcn_update_dpp(0, __builtin_bit_cast(int, x), ctrl, rmask, 0xF, false))
; __device__ __forceinline__ float wave_sum(float v) {
;     ...
;     v += WS_DPP(v, 0xB1, 0xF);
;     v += WS_DPP(v, 0x4E, 0xF);
;     v += WS_DPP(v, 0x141, 0xF);
;     v += WS_DPP(v, 0x140, 0xF);
;     v += WS_DPP(v, 0x142, 0xA);
;     v += WS_DPP(v, 0x143, 0xC);
;     ...
;     return __builtin_bit_cast(float, __builtin_amdgcn_readlane(__builtin_bit_cast(int, v), 63));
; template <int R, bool RT = false>
; __device__ __forceinline__ void norm_phase(const NormArgs& a, LAS unsigned char* lds, bool ctx_rows, const float* ctx_src, const float* ctx_shift, const float* ctx_scale) {
;     ...
;             for (int q = 0; q < R; ++q) { float ss = 0.f;
; #pragma unroll
;                 for (int j = 0; j < 4; ++j) ss += (v[q][j][0] * v[q][j][0] + v[q][j][1] * v[q][j][1]) + (v[q][j][2] * v[q][j][2] + v[q][j][3] * v[q][j][3]);
;                 rstd[q] = __builtin_amdgcn_rsqf(wave_sum(ss) * (1.f / DM) + EPS);
;                 if constexpr (RT) rsel[q] = ((lane >> 4) == rr / 4) ? rstd[q] : rsel[q]; }
; #pragma unroll
;             for (int q = 0; q < R; ++q) { const int row = row0 + rr + q;
; #pragma unroll
;                 for (int j = 0; j < 4; ++j) v[q][j] = (v[q][j] * rstd[q]) * A[j] + Sh[j];
	v_mul_f32_e32 v172, v125, v125
	v_mul_f32_e32 v174, v127, v127
	v_mov_b32_e32 v133, v179
	v_mov_b32_e32 v137, v180
	v_pk_add_f32 v[134:135], v[138:139], v[142:143]
	v_pk_add_f32 v[138:139], v[140:141], v[146:147]
	v_mov_b32_e32 v145, v183
	v_mov_b32_e32 v149, v184
	v_pk_add_f32 v[140:141], v[150:151], v[154:155]
	v_pk_add_f32 v[142:143], v[152:153], v[158:159]
	v_pk_add_f32 v[146:147], v[162:163], v[166:167]
	v_pk_add_f32 v[150:151], v[164:165], v[170:171]
	v_pk_add_f32 v[130:131], v[130:131], v[130:131] op_sel:[0,1] op_sel_hi:[1,0]
	v_pk_add_f32 v[128:129], v[128:129], v[128:129] op_sel:[0,1] op_sel_hi:[1,0]
	v_mul_f32_e32 v181, v92, v92
	v_mul_f32_e32 v182, v93, v93
	v_mul_f32_e32 v185, v108, v108
	v_mul_f32_e32 v186, v109, v109
	v_mul_f32_e32 v187, v110, v110
	v_mul_f32_e32 v188, v111, v111
	v_mul_f32_e32 v189, v18, v18
	v_mul_f32_e32 v190, v19, v19
	v_mul_f32_e32 v191, v20, v20
	v_mul_f32_e32 v192, v21, v21
	v_pk_fma_f32 v[168:169], v[124:125], v[124:125], v[172:173] op_sel_hi:[1,1,0]
	v_pk_fma_f32 v[172:173], v[126:127], v[126:127], v[174:175] op_sel_hi:[1,1,0]
	v_pk_add_f32 v[132:133], v[132:133], v[136:137]
	v_pk_add_f32 v[134:135], v[134:135], v[134:135] op_sel:[0,1] op_sel_hi:[1,0]
	v_pk_add_f32 v[136:137], v[138:139], v[138:139] op_sel:[0,1] op_sel_hi:[1,0]
	v_pk_add_f32 v[138:139], v[144:145], v[148:149]
	v_pk_add_f32 v[140:141], v[140:141], v[140:141] op_sel:[0,1] op_sel_hi:[1,0]
	v_pk_add_f32 v[142:143], v[142:143], v[142:143] op_sel:[0,1] op_sel_hi:[1,0]
	v_pk_add_f32 v[146:147], v[146:147], v[146:147] op_sel:[0,1] op_sel_hi:[1,0]
	v_pk_add_f32 v[148:149], v[150:151], v[150:151] op_sel:[0,1] op_sel_hi:[1,0]
	v_mov_b32_e32 v131, v175
	v_mov_b32_e32 v129, v178
	v_mov_b32_e32 v157, v187
	v_mov_b32_e32 v161, v188
	v_mov_b32_e32 v169, v191
	v_mov_b32_e32 v173, v192
	v_mov_b32_e32 v135, v181
	v_mov_b32_e32 v137, v182
	v_mov_b32_e32 v141, v185
	v_mov_b32_e32 v143, v186
	v_mov_b32_e32 v147, v189
	v_mov_b32_e32 v149, v190
	v_pk_add_f32 v[128:129], v[130:131], v[128:129]
	v_pk_add_f32 v[144:145], v[156:157], v[160:161]
	v_pk_add_f32 v[150:151], v[168:169], v[172:173]
	v_pk_add_f32 v[130:131], v[134:135], v[136:137]
	v_pk_add_f32 v[134:135], v[140:141], v[142:143]
	v_pk_add_f32 v[136:137], v[146:147], v[148:149]
	v_pk_add_f32 v[128:129], v[128:129], v[132:133]
	v_pk_add_f32 v[130:131], v[130:131], v[138:139]
	v_pk_add_f32 v[132:133], v[134:135], v[144:145]
	v_pk_add_f32 v[134:135], v[136:137], v[150:151]
	v_add_f32_e32 v128, v128, v129
	v_add_f32_e32 v129, v130, v131
	v_add_f32_e32 v130, v132, v133
	v_add_f32_e32 v131, v134, v135
	v_add_f32_dpp v128, v128, v128 quad_perm:[1,0,3,2] row_mask:0xf bank_mask:0xf bound_ctrl:1
	v_add_f32_dpp v129, v129, v129 quad_perm:[1,0,3,2] row_mask:0xf bank_mask:0xf bound_ctrl:1
	v_add_f32_dpp v130, v130, v130 quad_perm:[1,0,3,2] row_mask:0xf bank_mask:0xf bound_ctrl:1
	v_add_f32_dpp v131, v131, v131 quad_perm:[1,0,3,2] row_mask:0xf bank_mask:0xf bound_ctrl:1
	v_add_f32_dpp v128, v128, v128 quad_perm:[2,3,0,1] row_mask:0xf bank_mask:0xf bound_ctrl:1
	v_add_f32_dpp v129, v129, v129 quad_perm:[2,3,0,1] row_mask:0xf bank_mask:0xf bound_ctrl:1
	v_add_f32_dpp v130, v130, v130 quad_perm:[2,3,0,1] row_mask:0xf bank_mask:0xf bound_ctrl:1
	v_add_f32_dpp v131, v131, v131 quad_perm:[2,3,0,1] row_mask:0xf bank_mask:0xf bound_ctrl:1
	v_add_f32_dpp v128, v128, v128 row_half_mirror row_mask:0xf bank_mask:0xf bound_ctrl:1
	v_add_f32_dpp v129, v129, v129 row_half_mirror row_mask:0xf bank_mask:0xf bound_ctrl:1
	v_add_f32_dpp v130, v130, v130 row_half_mirror row_mask:0xf bank_mask:0xf bound_ctrl:1
	v_add_f32_dpp v131, v131, v131 row_half_mirror row_mask:0xf bank_mask:0xf bound_ctrl:1
	v_add_f32_dpp v128, v128, v128 row_mirror row_mask:0xf bank_mask:0xf bound_ctrl:1
	v_add_f32_dpp v129, v129, v129 row_mirror row_mask:0xf bank_mask:0xf bound_ctrl:1
	v_add_f32_dpp v130, v130, v130 row_mirror row_mask:0xf bank_mask:0xf bound_ctrl:1
	v_add_f32_dpp v131, v131, v131 row_mirror row_mask:0xf bank_mask:0xf bound_ctrl:1
	v_mov_b32_dpp v61, v128 row_bcast:15 row_mask:0xa bank_mask:0xf
	v_mov_b32_dpp v63, v129 row_bcast:15 row_mask:0xa bank_mask:0xf
	v_mov_b32_dpp v65, v130 row_bcast:15 row_mask:0xa bank_mask:0xf
	v_mov_b32_dpp v67, v131 row_bcast:15 row_mask:0xa bank_mask:0xf
	v_add_f32_e32 v61, v128, v61
	v_add_f32_e32 v63, v129, v63
	v_add_f32_e32 v65, v130, v65
	v_add_f32_e32 v67, v131, v67
	v_mov_b32_dpp v60, v61 row_bcast:31 row_mask:0xc bank_mask:0xf
	v_mov_b32_dpp v62, v63 row_bcast:31 row_mask:0xc bank_mask:0xf
	v_mov_b32_dpp v64, v65 row_bcast:31 row_mask:0xc bank_mask:0xf
	v_mov_b32_dpp v66, v67 row_bcast:31 row_mask:0xc bank_mask:0xf
	v_add_f32_e32 v60, v61, v60
	v_add_f32_e32 v61, v63, v62
	v_add_f32_e32 v62, v65, v64
	v_add_f32_e32 v63, v67, v66
	v_readlane_b32 s9, v60, 63
	v_readlane_b32 s11, v61, 63
	v_readlane_b32 s13, v62, 63
	v_readlane_b32 s31, v63, 63
	v_fma_f32 v60, s9, v59, v58
	v_fma_f32 v61, s11, v59, v58
	v_fma_f32 v63, s13, v59, v58
	v_fma_f32 v65, s31, v59, v58
	v_rsq_f32_e32 v60, v60
	v_rsq_f32_e32 v62, v61
	v_rsq_f32_e32 v64, v63
	v_rsq_f32_e32 v66, v65
	v_pk_mul_f32 v[68:69], v[68:69], v[60:61] op_sel_hi:[1,0]
	v_pk_mul_f32 v[70:71], v[70:71], v[60:61] op_sel_hi:[1,0]
	v_pk_mul_f32 v[72:73], v[72:73], v[60:61] op_sel_hi:[1,0]
	v_pk_mul_f32 v[74:75], v[74:75], v[60:61] op_sel_hi:[1,0]
	v_pk_mul_f32 v[80:81], v[80:81], v[60:61] op_sel_hi:[1,0]
	v_pk_mul_f32 v[82:83], v[82:83], v[60:61] op_sel_hi:[1,0]
; __device__ __forceinline__ unsigned pkb(float lo, float hi) { f32x2 v = {lo, hi}; bf16x2_t b = __builtin_convertvector(v, bf16x2_t); return __builtin_bit_cast(unsigned, b); }
; template <int R, bool RT = false>
; __device__ __forceinline__ void norm_phase(const NormArgs& a, LAS unsigned char* lds, bool ctx_rows, const float* ctx_src, const float* ctx_shift, const float* ctx_scale) {
;     ...
;     for (int chunk = gw; chunk < NTOK / 16; chunk += NGW) {
;     ...
;             for (int q = 0; q < R; ++q) { const int row = row0 + rr + q;
; #pragma unroll
;                 for (int j = 0; j < 4; ++j) v[q][j] = (v[q][j] * rstd[q]) * A[j] + Sh[j];
;                 if (a.fout) {
; #pragma unroll
;                     for (int j = 0; j < 4; ++j) *(f32x4*)(a.fout + (size_t)row * DM + 4 * lane + 256 * j) = v[q][j];
;                 }
;                 if (a.hout) {
; #pragma unroll
;                     for (int j = 0; j < 4; ++j) { u32x2 w; if (a.hbf) { w.x = pkb(v[q][j][0], v[q][j][1]); w.y = pkb(v[q][j][2], v[q][j][3]); } else { w.x = pkh(v[q][j][0], v[q][j][1]); w.y = pkh(v[q][j][2], v[q][j][3]); } *(u32x2*)(a.hout + (size_t)row * DM + 4 * lane + 256 * j) = w; }
;                 }
	v_pk_mul_f32 v[76:77], v[76:77], v[60:61] op_sel_hi:[1,0]
	v_pk_mul_f32 v[60:61], v[78:79], v[60:61] op_sel_hi:[1,0]
	v_pk_mul_f32 v[78:79], v[84:85], v[62:63] op_sel_hi:[1,0]
	v_pk_mul_f32 v[84:85], v[86:87], v[62:63] op_sel_hi:[1,0]
	v_pk_mul_f32 v[86:87], v[88:89], v[62:63] op_sel_hi:[1,0]
	v_pk_mul_f32 v[88:89], v[90:91], v[62:63] op_sel_hi:[1,0]
	v_pk_mul_f32 v[90:91], v[96:97], v[62:63] op_sel_hi:[1,0]
	v_pk_mul_f32 v[96:97], v[98:99], v[62:63] op_sel_hi:[1,0]
	v_pk_mul_f32 v[92:93], v[92:93], v[62:63] op_sel_hi:[1,0]
	v_pk_mul_f32 v[62:63], v[94:95], v[62:63] op_sel_hi:[1,0]
	v_pk_mul_f32 v[94:95], v[100:101], v[64:65] op_sel_hi:[1,0]
	v_pk_mul_f32 v[98:99], v[102:103], v[64:65] op_sel_hi:[1,0]
	v_pk_mul_f32 v[100:101], v[104:105], v[64:65] op_sel_hi:[1,0]
	v_pk_mul_f32 v[102:103], v[106:107], v[64:65] op_sel_hi:[1,0]
	v_pk_mul_f32 v[104:105], v[112:113], v[64:65] op_sel_hi:[1,0]
	v_pk_mul_f32 v[106:107], v[114:115], v[64:65] op_sel_hi:[1,0]
	v_pk_mul_f32 v[108:109], v[108:109], v[64:65] op_sel_hi:[1,0]
	v_pk_mul_f32 v[64:65], v[110:111], v[64:65] op_sel_hi:[1,0]
	v_pk_mul_f32 v[110:111], v[116:117], v[66:67] op_sel_hi:[1,0]
	v_pk_mul_f32 v[112:113], v[118:119], v[66:67] op_sel_hi:[1,0]
	v_pk_mul_f32 v[114:115], v[120:121], v[66:67] op_sel_hi:[1,0]
	v_pk_mul_f32 v[116:117], v[122:123], v[66:67] op_sel_hi:[1,0]
	v_pk_mul_f32 v[118:119], v[124:125], v[66:67] op_sel_hi:[1,0]
	v_pk_mul_f32 v[120:121], v[126:127], v[66:67] op_sel_hi:[1,0]
	v_pk_mul_f32 v[18:19], v[18:19], v[66:67] op_sel_hi:[1,0]
	v_pk_mul_f32 v[20:21], v[20:21], v[66:67] op_sel_hi:[1,0]
	v_pk_fma_f32 v[66:67], v[32:33], v[70:71], v[4:5]
	v_pk_fma_f32 v[68:69], v[34:35], v[68:69], v[2:3]
	v_pk_fma_f32 v[70:71], v[36:37], v[74:75], v[8:9]
	v_pk_fma_f32 v[72:73], v[38:39], v[72:73], v[6:7]
	v_pk_fma_f32 v[74:75], v[40:41], v[82:83], v[12:13]
	v_pk_fma_f32 v[80:81], v[42:43], v[80:81], v[10:11]
	v_pk_fma_f32 v[60:61], v[44:45], v[60:61], v[16:17]
	v_pk_fma_f32 v[76:77], v[46:47], v[76:77], v[14:15]
	v_pk_fma_f32 v[82:83], v[32:33], v[84:85], v[4:5]
	v_pk_fma_f32 v[78:79], v[34:35], v[78:79], v[2:3]
	v_pk_fma_f32 v[84:85], v[36:37], v[88:89], v[8:9]
	v_pk_fma_f32 v[86:87], v[38:39], v[86:87], v[6:7]
	v_pk_fma_f32 v[88:89], v[40:41], v[96:97], v[12:13]
	v_pk_fma_f32 v[90:91], v[42:43], v[90:91], v[10:11]
	v_pk_fma_f32 v[62:63], v[44:45], v[62:63], v[16:17]
	v_pk_fma_f32 v[92:93], v[46:47], v[92:93], v[14:15]
	v_pk_fma_f32 v[96:97], v[32:33], v[98:99], v[4:5]
	v_pk_fma_f32 v[94:95], v[34:35], v[94:95], v[2:3]
	v_pk_fma_f32 v[98:99], v[36:37], v[102:103], v[8:9]
	v_pk_fma_f32 v[100:101], v[38:39], v[100:101], v[6:7]
	v_pk_fma_f32 v[102:103], v[40:41], v[106:107], v[12:13]
	v_pk_fma_f32 v[104:105], v[42:43], v[104:105], v[10:11]
	v_pk_fma_f32 v[64:65], v[44:45], v[64:65], v[16:17]
	v_pk_fma_f32 v[106:107], v[46:47], v[108:109], v[14:15]
	v_pk_fma_f32 v[108:109], v[32:33], v[112:113], v[4:5]
	v_pk_fma_f32 v[110:111], v[34:35], v[110:111], v[2:3]
	v_pk_fma_f32 v[112:113], v[36:37], v[116:117], v[8:9]
	v_pk_fma_f32 v[114:115], v[38:39], v[114:115], v[6:7]
	v_pk_fma_f32 v[116:117], v[40:41], v[120:121], v[12:13]
	v_pk_fma_f32 v[118:119], v[42:43], v[118:119], v[10:11]
	v_pk_fma_f32 v[20:21], v[44:45], v[20:21], v[16:17]
	v_pk_fma_f32 v[18:19], v[46:47], v[18:19], v[14:15]
	v_cvt_pk_f16_f32 v68, v68, v69
	v_cvt_pk_f16_f32 v69, v66, v67
	v_cvt_pk_f16_f32 v66, v72, v73
	v_cvt_pk_f16_f32 v67, v70, v71
	v_cvt_pk_f16_f32 v70, v80, v81
	v_cvt_pk_f16_f32 v71, v74, v75
	v_cvt_pk_f16_f32 v72, v76, v77
	v_cvt_pk_f16_f32 v73, v60, v61
	v_cvt_pk_f16_f32 v60, v78, v79
	v_cvt_pk_f16_f32 v61, v82, v83
	v_cvt_pk_f16_f32 v74, v86, v87
	v_cvt_pk_f16_f32 v75, v84, v85
	v_cvt_pk_f16_f32 v76, v90, v91
	v_cvt_pk_f16_f32 v77, v88, v89
	v_cvt_pk_f16_f32 v78, v92, v93
	v_cvt_pk_f16_f32 v79, v62, v63
	v_cvt_pk_f16_f32 v62, v94, v95
	v_cvt_pk_f16_f32 v63, v96, v97
	v_cvt_pk_f16_f32 v80, v100, v101
	v_cvt_pk_f16_f32 v81, v98, v99
	v_cvt_pk_f16_f32 v82, v104, v105
	v_cvt_pk_f16_f32 v83, v102, v103
	v_cvt_pk_f16_f32 v84, v106, v107
	v_cvt_pk_f16_f32 v85, v64, v65
	v_cvt_pk_f16_f32 v64, v110, v111
	v_cvt_pk_f16_f32 v65, v108, v109
	v_cvt_pk_f16_f32 v86, v114, v115
	v_cvt_pk_f16_f32 v87, v112, v113
	v_cvt_pk_f16_f32 v88, v118, v119
	v_cvt_pk_f16_f32 v89, v116, v117
	v_cvt_pk_f16_f32 v18, v18, v19
	v_cvt_pk_f16_f32 v19, v20, v21
	global_store_dwordx2 v[54:55], v[68:69], off
	global_store_dwordx2 v[54:55], v[66:67], off offset:512
	global_store_dwordx2 v[54:55], v[70:71], off offset:1024
	global_store_dwordx2 v[54:55], v[72:73], off offset:1536
	global_store_dwordx2 v[52:53], v[60:61], off
	global_store_dwordx2 v[52:53], v[74:75], off offset:512
	global_store_dwordx2 v[52:53], v[76:77], off offset:1024
	global_store_dwordx2 v[52:53], v[78:79], off offset:1536
	global_store_dwordx2 v[50:51], v[62:63], off
	global_store_dwordx2 v[50:51], v[80:81], off offset:512
	global_store_dwordx2 v[50:51], v[82:83], off offset:1024
	global_store_dwordx2 v[50:51], v[84:85], off offset:1536
	global_store_dwordx2 v[48:49], v[64:65], off
	global_store_dwordx2 v[48:49], v[86:87], off offset:512
	global_store_dwordx2 v[48:49], v[88:89], off offset:1024
	global_store_dwordx2 v[48:49], v[18:19], off offset:1536
	s_cbranch_scc0 .LBB0_308
	s_add_i32 s30, s30, s6
	s_add_i32 s2, s2, s5
	s_add_i32 s8, s8, s5
	s_add_i32 s10, s10, s5
	s_add_i32 s12, s12, s5
	s_cmpk_gt_i32 s30, 0x7ff
	s_cbranch_scc0 .LBB0_307

;     __device__ __forceinline__ void operator()(const Acc& acc, const Unit& u, int wr, int wc, int fr, int fq) const {
;         const int col0 = u.pn * BM + wc * 32 + 8 * fq; const int b = (u.pm * BM) / SEQ;
;         f32x4 gv[2][2];
; #pragma unroll
;         for (int bj = 0; bj < 2; ++bj)
; #pragma unroll
;             for (int n = 0; n < 2; ++n) gv[bj][n] = *(const f32x4*)(gate + (size_t)b * gstride + col0 + bj * HALF + 4 * n);
; #pragma unroll
;         for (int ai = 0; ai < 2; ++ai)
; #pragma unroll
;             for (int m = 0; m < 4; ++m) { const size_t off = (size_t)(u.pm * BM + ai * HALF + wr * 64 + m * 16 + fr) * DM + col0;
; #pragma unroll
;                 for (int bj = 0; bj < 2; ++bj) { f32x4 b0, b1;
;                     if constexpr (BASE16) { const f16x8 bv = *(const f16x8*)((const f16*)base + off + bj * HALF);
;                         b0 = (f32x4){(float)bv[0], (float)bv[1], (float)bv[2], (float)bv[3]}; b1 = (f32x4){(float)bv[4], (float)bv[5], (float)bv[6], (float)bv[7]}; }
;                     else { b0 = *(const f32x4*)((const float*)base + off + bj * HALF); b1 = *(const f32x4*)((const float*)base + off + bj * HALF + 4); }
;                     const f32x4 v0 = b0 + gv[bj][0] * acc[ai][bj][m][0], v1 = b1 + gv[bj][1] * acc[ai][bj][m][1];
;                     u32x4 w; w.x = pkh(v0[0], v0[1]); w.y = pkh(v0[2], v0[3]); w.z = pkh(v1[0], v1[1]); w.w = pkh(v1[2], v1[3]);
;                     *(u32x4*)(out + off + bj * HALF) = w; }
;                 if (m & 1) asm volatile("" ::: "memory"); }
.LBB0_718:
	v_lshl_or_b32 v162, s3, 8, v167
	s_ashr_i32 s3, s2, 31
	s_lshr_b32 s3, s3, 29
	s_add_i32 s3, s2, s3
	s_ashr_i32 s3, s3, 3
	v_lshl_add_u32 v164, s2, 8, v1
	s_mul_hi_i32 s13, s3, 0x6000
	s_mulk_i32 s3, 0x6000
	v_ashrrev_i32_e32 v165, 31, v164
	s_add_u32 s20, s36, s3
	v_ashrrev_i32_e32 v163, 31, v162
	v_lshlrev_b64 v[134:135], 10, v[164:165]
	v_readlane_b32 s44, v251, 60
	s_addc_u32 s21, s37, s13
	v_lshl_add_u64 v[138:139], v[134:135], 0, v[162:163]
	v_readlane_b32 s45, v251, 61
	v_lshl_add_u64 v[142:143], v[162:163], 2, s[20:21]
	global_load_dwordx4 v[130:133], v[142:143], off
	v_lshl_add_u64 v[180:181], v[138:139], 2, s[44:45]
	global_load_dwordx4 v[172:175], v[180:181], off nt
	global_load_dwordx4 v[176:179], v[180:181], off offset:16 nt
	global_load_dwordx4 v[134:137], v[142:143], off offset:16
	v_lshl_add_u64 v[182:183], v[138:139], 1, s[66:67]
	global_load_dwordx4 v[138:141], v[142:143], off offset:528
	s_nop 0
	global_load_dwordx4 v[142:145], v[142:143], off offset:512
	s_andn2_b64 vcc, exec, s[4:5]
	s_mov_b64 s[2:3], -1
	v_readlane_b32 s46, v251, 62
	v_readlane_b32 s47, v251, 63
	v_readlane_b32 s48, v250, 0
	v_readlane_b32 s49, v250, 1
	v_readlane_b32 s50, v250, 2
	v_readlane_b32 s51, v250, 3
	v_readlane_b32 s52, v250, 4
	v_readlane_b32 s53, v250, 5
	v_readlane_b32 s54, v250, 6
	v_readlane_b32 s55, v250, 7
	v_readlane_b32 s56, v250, 8
	v_readlane_b32 s57, v250, 9
	v_readlane_b32 s58, v250, 10
	v_readlane_b32 s59, v250, 11
	s_waitcnt vmcnt(0)
	v_pk_fma_f32 v[128:129], v[128:129], v[132:133], v[174:175]
	v_pk_fma_f32 v[126:127], v[126:127], v[130:131], v[172:173]
	v_pk_fma_f32 v[172:173], v[124:125], v[136:137], v[178:179]
	v_pk_fma_f32 v[124:125], v[122:123], v[134:135], v[176:177]
	v_cvt_pk_f16_f32 v122, v126, v127
	v_cvt_pk_f16_f32 v123, v128, v129
	v_cvt_pk_f16_f32 v124, v124, v125
	v_cvt_pk_f16_f32 v125, v172, v173
	global_store_dwordx4 v[182:183], v[122:125], off
	global_load_dwordx4 v[122:125], v[180:181], off offset:512 nt
	s_nop 0
	global_load_dwordx4 v[126:129], v[180:181], off offset:528 nt
	v_or_b32_e32 v172, 16, v164
	v_ashrrev_i32_e32 v173, 31, v172
	v_lshlrev_b64 v[172:173], 10, v[172:173]
	v_lshl_add_u64 v[172:173], v[172:173], 0, v[162:163]
	v_lshl_add_u64 v[174:175], v[172:173], 2, s[44:45]
	s_waitcnt vmcnt(1)
	v_pk_fma_f32 v[120:121], v[120:121], v[144:145], v[124:125]
	v_pk_fma_f32 v[118:119], v[118:119], v[142:143], v[122:123]
	s_waitcnt vmcnt(0)
	v_pk_fma_f32 v[122:123], v[116:117], v[140:141], v[128:129]
	v_pk_fma_f32 v[116:117], v[114:115], v[138:139], v[126:127]
	v_cvt_pk_f16_f32 v114, v118, v119
	v_cvt_pk_f16_f32 v115, v120, v121
	v_cvt_pk_f16_f32 v116, v116, v117
	v_cvt_pk_f16_f32 v117, v122, v123
	global_store_dwordx4 v[182:183], v[114:117], off offset:256
	global_load_dwordx4 v[114:117], v[174:175], off nt
	s_nop 0
	global_load_dwordx4 v[118:121], v[174:175], off offset:16 nt
	v_lshl_add_u64 v[122:123], v[172:173], 1, s[66:67]
	s_waitcnt vmcnt(1)
	v_pk_fma_f32 v[112:113], v[112:113], v[132:133], v[116:117]
	v_pk_fma_f32 v[110:111], v[110:111], v[130:131], v[114:115]
	s_waitcnt vmcnt(0)
	v_pk_fma_f32 v[114:115], v[108:109], v[136:137], v[120:121]
	v_pk_fma_f32 v[108:109], v[106:107], v[134:135], v[118:119]
	v_cvt_pk_f16_f32 v106, v110, v111
	v_cvt_pk_f16_f32 v107, v112, v113
	v_cvt_pk_f16_f32 v108, v108, v109
	v_cvt_pk_f16_f32 v109, v114, v115
	global_store_dwordx4 v[122:123], v[106:109], off
	global_load_dwordx4 v[106:109], v[174:175], off offset:512 nt
	s_nop 0
	global_load_dwordx4 v[110:113], v[174:175], off offset:528 nt
	v_or_b32_e32 v114, 32, v164
	v_ashrrev_i32_e32 v115, 31, v114
	v_lshlrev_b64 v[114:115], 10, v[114:115]
	v_lshl_add_u64 v[114:115], v[114:115], 0, v[162:163]
	v_lshl_add_u64 v[116:117], v[114:115], 2, s[44:45]
	s_waitcnt vmcnt(1)
	v_pk_fma_f32 v[104:105], v[104:105], v[144:145], v[108:109]
	v_pk_fma_f32 v[102:103], v[102:103], v[142:143], v[106:107]
	s_waitcnt vmcnt(0)
	v_pk_fma_f32 v[106:107], v[100:101], v[140:141], v[112:113]
	v_pk_fma_f32 v[100:101], v[98:99], v[138:139], v[110:111]
	v_cvt_pk_f16_f32 v98, v102, v103
	v_cvt_pk_f16_f32 v99, v104, v105
	v_cvt_pk_f16_f32 v100, v100, v101
	v_cvt_pk_f16_f32 v101, v106, v107
	global_store_dwordx4 v[122:123], v[98:101], off offset:256
	global_load_dwordx4 v[98:101], v[116:117], off nt
	global_load_dwordx4 v[102:105], v[116:117], off offset:16 nt
	v_lshl_add_u64 v[106:107], v[114:115], 1, s[66:67]
	s_waitcnt vmcnt(1)
	v_pk_fma_f32 v[96:97], v[96:97], v[132:133], v[100:101]
	v_pk_fma_f32 v[94:95], v[94:95], v[130:131], v[98:99]
	s_waitcnt vmcnt(0)
	v_pk_fma_f32 v[98:99], v[92:93], v[136:137], v[104:105]
	v_pk_fma_f32 v[92:93], v[90:91], v[134:135], v[102:103]
	v_cvt_pk_f16_f32 v90, v94, v95
	v_cvt_pk_f16_f32 v91, v96, v97
	v_cvt_pk_f16_f32 v92, v92, v93
	v_cvt_pk_f16_f32 v93, v98, v99
	global_store_dwordx4 v[106:107], v[90:93], off
	global_load_dwordx4 v[90:93], v[116:117], off offset:512 nt
	s_nop 0
	global_load_dwordx4 v[94:97], v[116:117], off offset:528 nt
	v_or_b32_e32 v98, 48, v164
	v_ashrrev_i32_e32 v99, 31, v98
	v_lshlrev_b64 v[98:99], 10, v[98:99]
	v_lshl_add_u64 v[98:99], v[98:99], 0, v[162:163]
	v_lshl_add_u64 v[100:101], v[98:99], 2, s[44:45]
	s_waitcnt vmcnt(1)
	v_pk_fma_f32 v[88:89], v[88:89], v[144:145], v[92:93]
	v_pk_fma_f32 v[86:87], v[86:87], v[142:143], v[90:91]
	s_waitcnt vmcnt(0)
	v_pk_fma_f32 v[90:91], v[84:85], v[140:141], v[96:97]
	v_pk_fma_f32 v[84:85], v[82:83], v[138:139], v[94:95]
	v_cvt_pk_f16_f32 v82, v86, v87
	v_cvt_pk_f16_f32 v83, v88, v89
	v_cvt_pk_f16_f32 v84, v84, v85
	v_cvt_pk_f16_f32 v85, v90, v91
	global_store_dwordx4 v[106:107], v[82:85], off offset:256
	global_load_dwordx4 v[82:85], v[100:101], off nt
	s_nop 0
	global_load_dwordx4 v[86:89], v[100:101], off offset:16 nt
	v_lshl_add_u64 v[90:91], v[98:99], 1, s[66:67]
	s_waitcnt vmcnt(1)
; #define GM_BAR __builtin_amdgcn_s_barrier()
;     __device__ __forceinline__ void operator()(const Acc& acc, const Unit& u, int wr, int wc, int fr, int fq) const {
;     ...
;             for (int m = 0; m < 4; ++m) { const size_t off = (size_t)(u.pm * BM + ai * HALF + wr * 64 + m * 16 + fr) * DM + col0;
; #pragma unroll
;                 for (int bj = 0; bj < 2; ++bj) { f32x4 b0, b1;
;                     if constexpr (BASE16) { const f16x8 bv = *(const f16x8*)((const f16*)base + off + bj * HALF);
;                         b0 = (f32x4){(float)bv[0], (float)bv[1], (float)bv[2], (float)bv[3]}; b1 = (f32x4){(float)bv[4], (float)bv[5], (float)bv[6], (float)bv[7]}; }
;                     else { b0 = *(const f32x4*)((const float*)base + off + bj * HALF); b1 = *(const f32x4*)((const float*)base + off + bj * HALF + 4); }
;                     const f32x4 v0 = b0 + gv[bj][0] * acc[ai][bj][m][0], v1 = b1 + gv[bj][1] * acc[ai][bj][m][1];
;                     u32x4 w; w.x = pkh(v0[0], v0[1]); w.y = pkh(v0[2], v0[3]); w.z = pkh(v1[0], v1[1]); w.w = pkh(v1[2], v1[3]);
;                     *(u32x4*)(out + off + bj * HALF) = w; }
;                 if (m & 1) asm volatile("" ::: "memory"); }
; template <bool BF, bool GATHER = false, class Epi, class Hook>
; __device__ __forceinline__ void gemm_phase(LAS unsigned char* lds, const Gemm g, const Order& S, const Epi& E, Hook& HK) {
;     ...
;         if (!has_next) break;
; #pragma unroll
;         for (int a = 0; a < 2; ++a)
; #pragma unroll
;             for (int b = 0; b < 2; ++b)
; #pragma unroll
;                 for (int m = 0; m < 4; ++m)
; #pragma unroll
;                     for (int n = 0; n < 2; ++n) acc[a][b][m][n] = (f32x4){0.f, 0.f, 0.f, 0.f};
;         cur = nxt; cA = nA; cB = nB; ++ui;
;         if constexpr (GATHER) { gA0[0] = nA0[0]; gA0[1] = nA0[1]; gA1[0] = nA1[0]; gA1[1] = nA1[1]; }
;         if (wr == 1) GM_BAR;
	v_pk_fma_f32 v[80:81], v[80:81], v[132:133], v[84:85]
	v_pk_fma_f32 v[78:79], v[78:79], v[130:131], v[82:83]
	s_waitcnt vmcnt(0)
	v_pk_fma_f32 v[82:83], v[76:77], v[136:137], v[88:89]
	v_pk_fma_f32 v[76:77], v[74:75], v[134:135], v[86:87]
	v_cvt_pk_f16_f32 v74, v78, v79
	v_cvt_pk_f16_f32 v75, v80, v81
	v_cvt_pk_f16_f32 v76, v76, v77
	v_cvt_pk_f16_f32 v77, v82, v83
	global_store_dwordx4 v[90:91], v[74:77], off
	global_load_dwordx4 v[74:77], v[100:101], off offset:512 nt
	s_nop 0
	global_load_dwordx4 v[78:81], v[100:101], off offset:528 nt
	v_add_u32_e32 v82, 0x80, v164
	v_ashrrev_i32_e32 v83, 31, v82
	v_lshlrev_b64 v[82:83], 10, v[82:83]
	v_lshl_add_u64 v[82:83], v[82:83], 0, v[162:163]
	v_lshl_add_u64 v[84:85], v[82:83], 2, s[44:45]
	s_waitcnt vmcnt(1)
	v_pk_fma_f32 v[72:73], v[72:73], v[144:145], v[76:77]
	v_pk_fma_f32 v[70:71], v[70:71], v[142:143], v[74:75]
	s_waitcnt vmcnt(0)
	v_pk_fma_f32 v[74:75], v[68:69], v[140:141], v[80:81]
	v_pk_fma_f32 v[68:69], v[66:67], v[138:139], v[78:79]
	v_cvt_pk_f16_f32 v66, v70, v71
	v_cvt_pk_f16_f32 v67, v72, v73
	v_cvt_pk_f16_f32 v68, v68, v69
	v_cvt_pk_f16_f32 v69, v74, v75
	global_store_dwordx4 v[90:91], v[66:69], off offset:256
	global_load_dwordx4 v[66:69], v[84:85], off nt
	global_load_dwordx4 v[70:73], v[84:85], off offset:16 nt
	v_lshl_add_u64 v[74:75], v[82:83], 1, s[66:67]
	s_waitcnt vmcnt(1)
	v_pk_fma_f32 v[64:65], v[64:65], v[132:133], v[68:69]
	v_pk_fma_f32 v[62:63], v[62:63], v[130:131], v[66:67]
	s_waitcnt vmcnt(0)
	v_pk_fma_f32 v[66:67], v[60:61], v[136:137], v[72:73]
	v_pk_fma_f32 v[60:61], v[58:59], v[134:135], v[70:71]
	v_cvt_pk_f16_f32 v58, v62, v63
	v_cvt_pk_f16_f32 v59, v64, v65
	v_cvt_pk_f16_f32 v60, v60, v61
	v_cvt_pk_f16_f32 v61, v66, v67
	global_store_dwordx4 v[74:75], v[58:61], off
	global_load_dwordx4 v[58:61], v[84:85], off offset:512 nt
	s_nop 0
	global_load_dwordx4 v[62:65], v[84:85], off offset:528 nt
	v_add_u32_e32 v66, 0x90, v164
	v_ashrrev_i32_e32 v67, 31, v66
	v_lshlrev_b64 v[66:67], 10, v[66:67]
	v_lshl_add_u64 v[66:67], v[66:67], 0, v[162:163]
	v_lshl_add_u64 v[68:69], v[66:67], 2, s[44:45]
	s_waitcnt vmcnt(1)
	v_pk_fma_f32 v[56:57], v[56:57], v[144:145], v[60:61]
	v_pk_fma_f32 v[54:55], v[54:55], v[142:143], v[58:59]
	s_waitcnt vmcnt(0)
	v_pk_fma_f32 v[58:59], v[52:53], v[140:141], v[64:65]
	v_pk_fma_f32 v[52:53], v[50:51], v[138:139], v[62:63]
	v_cvt_pk_f16_f32 v50, v54, v55
	v_cvt_pk_f16_f32 v51, v56, v57
	v_cvt_pk_f16_f32 v52, v52, v53
	v_cvt_pk_f16_f32 v53, v58, v59
	global_store_dwordx4 v[74:75], v[50:53], off offset:256
	global_load_dwordx4 v[50:53], v[68:69], off nt
	s_nop 0
	global_load_dwordx4 v[54:57], v[68:69], off offset:16 nt
	v_lshl_add_u64 v[58:59], v[66:67], 1, s[66:67]
	s_waitcnt vmcnt(1)
	v_pk_fma_f32 v[48:49], v[48:49], v[132:133], v[52:53]
	v_pk_fma_f32 v[46:47], v[46:47], v[130:131], v[50:51]
	s_waitcnt vmcnt(0)
	v_pk_fma_f32 v[50:51], v[44:45], v[136:137], v[56:57]
	v_pk_fma_f32 v[44:45], v[42:43], v[134:135], v[54:55]
	v_cvt_pk_f16_f32 v42, v46, v47
	v_cvt_pk_f16_f32 v43, v48, v49
	v_cvt_pk_f16_f32 v44, v44, v45
	v_cvt_pk_f16_f32 v45, v50, v51
	global_store_dwordx4 v[58:59], v[42:45], off
	global_load_dwordx4 v[42:45], v[68:69], off offset:512 nt
	s_nop 0
	global_load_dwordx4 v[46:49], v[68:69], off offset:528 nt
	v_add_u32_e32 v50, 0xa0, v164
	v_ashrrev_i32_e32 v51, 31, v50
	v_lshlrev_b64 v[50:51], 10, v[50:51]
	v_lshl_add_u64 v[50:51], v[50:51], 0, v[162:163]
	v_lshl_add_u64 v[52:53], v[50:51], 2, s[44:45]
	s_waitcnt vmcnt(1)
	v_pk_fma_f32 v[40:41], v[40:41], v[144:145], v[44:45]
	v_pk_fma_f32 v[38:39], v[38:39], v[142:143], v[42:43]
	s_waitcnt vmcnt(0)
	v_pk_fma_f32 v[42:43], v[36:37], v[140:141], v[48:49]
	v_pk_fma_f32 v[36:37], v[34:35], v[138:139], v[46:47]
	v_cvt_pk_f16_f32 v34, v38, v39
	v_cvt_pk_f16_f32 v35, v40, v41
	v_cvt_pk_f16_f32 v36, v36, v37
	v_cvt_pk_f16_f32 v37, v42, v43
	global_store_dwordx4 v[58:59], v[34:37], off offset:256
	global_load_dwordx4 v[34:37], v[52:53], off nt
	global_load_dwordx4 v[38:41], v[52:53], off offset:16 nt
	v_lshl_add_u64 v[42:43], v[50:51], 1, s[66:67]
	s_waitcnt vmcnt(1)
	v_pk_fma_f32 v[32:33], v[32:33], v[132:133], v[36:37]
	v_pk_fma_f32 v[30:31], v[30:31], v[130:131], v[34:35]
	s_waitcnt vmcnt(0)
	v_pk_fma_f32 v[34:35], v[28:29], v[136:137], v[40:41]
	v_pk_fma_f32 v[28:29], v[26:27], v[134:135], v[38:39]
	v_cvt_pk_f16_f32 v26, v30, v31
	v_cvt_pk_f16_f32 v27, v32, v33
	v_cvt_pk_f16_f32 v28, v28, v29
	v_cvt_pk_f16_f32 v29, v34, v35
	global_store_dwordx4 v[42:43], v[26:29], off
	global_load_dwordx4 v[26:29], v[52:53], off offset:512 nt
	s_nop 0
	global_load_dwordx4 v[30:33], v[52:53], off offset:528 nt
	v_add_u32_e32 v34, 0xb0, v164
	v_ashrrev_i32_e32 v35, 31, v34
	v_lshlrev_b64 v[34:35], 10, v[34:35]
	v_lshl_add_u64 v[34:35], v[34:35], 0, v[162:163]
	v_lshl_add_u64 v[36:37], v[34:35], 2, s[44:45]
	s_waitcnt vmcnt(1)
	v_pk_fma_f32 v[24:25], v[24:25], v[144:145], v[28:29]
	v_pk_fma_f32 v[22:23], v[22:23], v[142:143], v[26:27]
	s_waitcnt vmcnt(0)
	v_pk_fma_f32 v[26:27], v[20:21], v[140:141], v[32:33]
	v_pk_fma_f32 v[20:21], v[18:19], v[138:139], v[30:31]
	v_cvt_pk_f16_f32 v18, v22, v23
	v_cvt_pk_f16_f32 v19, v24, v25
	v_cvt_pk_f16_f32 v20, v20, v21
	v_cvt_pk_f16_f32 v21, v26, v27
	global_store_dwordx4 v[42:43], v[18:21], off offset:256
	global_load_dwordx4 v[18:21], v[36:37], off nt
	s_nop 0
	global_load_dwordx4 v[22:25], v[36:37], off offset:16 nt
	v_lshl_add_u64 v[26:27], v[34:35], 1, s[66:67]
	s_waitcnt vmcnt(1)
	v_pk_fma_f32 v[16:17], v[16:17], v[132:133], v[20:21]
	v_pk_fma_f32 v[14:15], v[14:15], v[130:131], v[18:19]
	s_waitcnt vmcnt(0)
	v_pk_fma_f32 v[18:19], v[12:13], v[136:137], v[24:25]
	v_pk_fma_f32 v[12:13], v[10:11], v[134:135], v[22:23]
	v_cvt_pk_f16_f32 v10, v14, v15
	v_cvt_pk_f16_f32 v11, v16, v17
	v_cvt_pk_f16_f32 v12, v12, v13
	v_cvt_pk_f16_f32 v13, v18, v19
	global_store_dwordx4 v[26:27], v[10:13], off
	global_load_dwordx4 v[10:13], v[36:37], off offset:512 nt
	s_nop 0
	global_load_dwordx4 v[14:17], v[36:37], off offset:528 nt
	s_waitcnt vmcnt(1)
	v_pk_fma_f32 v[8:9], v[8:9], v[144:145], v[12:13]
	v_pk_fma_f32 v[6:7], v[6:7], v[142:143], v[10:11]
	s_waitcnt vmcnt(0)
	v_pk_fma_f32 v[10:11], v[4:5], v[140:141], v[16:17]
	v_pk_fma_f32 v[4:5], v[2:3], v[138:139], v[14:15]
	v_cvt_pk_f16_f32 v2, v6, v7
	v_cvt_pk_f16_f32 v3, v8, v9
	v_cvt_pk_f16_f32 v4, v4, v5
	v_cvt_pk_f16_f32 v5, v10, v11
	global_store_dwordx4 v[26:27], v[2:5], off offset:256
	s_cbranch_vccnz .LBB0_707
	s_andn2_b64 vcc, exec, s[6:7]
	s_cbranch_vccnz .LBB0_706
	s_barrier
	s_branch .LBB0_706

; #define LAS __attribute__((address_space(3)))
; template <int R, bool RT = false>
; __device__ __forceinline__ void norm_phase(const NormArgs& a, LAS unsigned char* lds, bool ctx_rows, const float* ctx_src, const float* ctx_shift, const float* ctx_scale) {
;     ...
;             for (int q = 0; q < R; ++q) { sl[q] = -1; if (a.y2) { const int r = rr + q; const int pk = r < 4 ? ipk[0] : (r < 8 ? ipk[1] : (r < 12 ? ipk[2] : ipk[3]));
;                     const int got = __shfl(pk, (lane & 15) + 16 * (r & 3)); sl[q] = lane < 16 ? got : -1; } }
; #pragma unroll
;             for (int q = 0; q < R; ++q) { const int row = row0 + rr + q;
;                 if (a.src16) { const f16* xr = a.src16 + (size_t)row * DM;
; #pragma unroll
;                     for (int j = 0; j < 4; ++j) { const f16x4 t = *(const f16x4*)(xr + 4 * lane + 256 * j); v[q][j] = (f32x4){(float)t[0], (float)t[1], (float)t[2], (float)t[3]};
;                         if constexpr (RT) { if (j == 0) *(LAS u32x2*)(hs + (rr + q) * 528 + 8 * lane) = __builtin_bit_cast(u32x2, t);
;                             else xp[rr / 4][q][j - 1] = __builtin_bit_cast(u32x2, t); } } }
;                 else { const float* xr = a.src + (size_t)row * DM;
; #pragma unroll
;                     for (int j = 0; j < 4; ++j) v[q][j] = *(const f32x4*)(xr + 4 * lane + 256 * j); } }
;             if (a.y2) {
;                 unsigned long long mask[R]; int ee[R][4]; float wgt[R][4]; f16x4 ld[R][4][4];
;                 int cnt[R];
; #pragma unroll
;                 for (int q = 0; q < R; ++q) { mask[q] = __ballot(sl[q] >= 0); cnt[q] = __builtin_popcountll(mask[q]);
; #pragma unroll
;                     for (int i = 0; i < 4; ++i) { if (mask[q]) { ee[q][i] = __builtin_ctzll(mask[q]); mask[q] &= mask[q] - 1; wgt[q][i] = 1.f; } else { ee[q][i] = i ? ee[q][0] : 0; wgt[q][i] = 0.f; } }
; #pragma unroll
;                     for (int i = 0; i < 4; ++i) {
;                         if (i < cnt[q]) { int slot = __shfl(sl[q], ee[q][i]); slot = slot < 0 ? 0 : slot; const f16* yr = a.y2 + ((size_t)ee[q][i] * EROWS + b * CAP + slot) * DM + 4 * lane;
; #pragma unroll
;                             for (int j = 0; j < 4; ++j) ld[q][i][j] = *(const f16x4*)(yr + 256 * j); } } }
.LBB0_1168:
	s_cmp_lt_u32 s36, 4
	s_cselect_b64 vcc, -1, 0
	s_cmp_lt_u32 s36, 8
	s_cselect_b64 s[0:1], -1, 0
	s_cmp_lt_u32 s36, 12
	s_cselect_b64 s[6:7], -1, 0
	s_or_b32 s2, s36, s33
	s_ashr_i32 s3, s2, 31
	s_lshl_b64 s[12:13], s[2:3], 11
	s_or_b32 s2, s2, 1
	s_ashr_i32 s3, s2, 31
	v_cndmask_b32_e64 v2, v182, v181, s[6:7]
	v_lshl_add_u64 v[4:5], v[56:57], 0, s[12:13]
	s_lshl_b64 s[6:7], s[2:3], 11
	global_load_dwordx2 v[164:165], v[4:5], off nt
	global_load_dwordx2 v[162:163], v[4:5], off offset:512 nt
	global_load_dwordx2 v[160:161], v[4:5], off offset:1024 nt
	global_load_dwordx2 v[158:159], v[4:5], off offset:1536 nt
	v_lshl_add_u64 v[4:5], v[56:57], 0, s[6:7]
	global_load_dwordx2 v[156:157], v[4:5], off nt
	global_load_dwordx2 v[154:155], v[4:5], off offset:512 nt
	global_load_dwordx2 v[152:153], v[4:5], off offset:1024 nt
	global_load_dwordx2 v[150:151], v[4:5], off offset:1536 nt
	v_cndmask_b32_e64 v2, v2, v180, s[0:1]
	s_lshl_b32 s0, s36, 4
	v_cndmask_b32_e32 v2, v2, v179, vcc
	v_and_or_b32 v4, s0, 32, v175
	v_bfe_i32 v2, v2, 0, 16
	v_lshlrev_b32_e32 v4, 2, v4
	ds_bpermute_b32 v5, v4, v2
	ds_bpermute_b32 v4, v4, v2 offset:64
	s_waitcnt lgkmcnt(1)
	v_cndmask_b32_e64 v166, -1, v5, s[4:5]
	v_cmp_lt_i32_e32 vcc, -1, v166
	s_cmp_eq_u64 vcc, 0
	s_cselect_b64 s[0:1], -1, 0
	s_cmp_lg_u64 vcc, 0
	s_cselect_b64 s[28:29], -1, 0
	s_ff1_i32_b64 s14, vcc
	s_cbranch_vccz .LBB0_1170
	v_or_b32_e32 v2, s14, v174
	v_lshlrev_b32_e32 v2, 2, v2
	ds_bpermute_b32 v2, v2, v166
	s_mov_b32 s15, s11
	s_lshl_b64 s[2:3], s[14:15], 12
	s_add_u32 s2, s2, s34
	s_addc_u32 s3, s3, s35
	s_waitcnt lgkmcnt(0)
	v_max_i32_e32 v2, 0, v2
	v_lshl_add_u64 v[6:7], s[2:3], 0, v[2:3]
	v_lshlrev_b64 v[6:7], 11, v[6:7]
	v_lshl_add_u64 v[6:7], v[58:59], 0, v[6:7]
	global_load_dwordx2 v[132:133], v[6:7], off nt
	global_load_dwordx2 v[130:131], v[6:7], off offset:512 nt
	global_load_dwordx2 v[128:129], v[6:7], off offset:1024 nt
	global_load_dwordx2 v[126:127], v[6:7], off offset:1536 nt
.LBB0_1170:
	s_bcnt1_i32_b64 s10, vcc
	s_add_u32 s2, vcc_lo, -1
	s_addc_u32 s3, vcc_hi, -1
	s_and_b64 s[2:3], s[2:3], vcc
	s_and_b64 s[0:1], s[0:1], exec
	v_cmp_lt_u64_e64 s[0:1], s[10:11], 2
	s_cselect_b32 s14, 0, s14
	v_cmp_gt_u64_e64 s[26:27], s[10:11], 1
	s_and_b64 vcc, exec, s[0:1]
	s_cbranch_vccnz .LBB0_1172
	s_cmp_eq_u64 s[2:3], 0
	s_ff1_i32_b64 s0, s[2:3]
	s_cselect_b32 s0, s14, s0
	v_or_b32_e32 v2, s0, v174
	v_lshlrev_b32_e32 v2, 2, v2
	ds_bpermute_b32 v2, v2, v166
	s_lshl_b32 s0, s0, 12
	s_add_u32 s0, s0, s34
	s_addc_u32 s1, 0, s35
	s_waitcnt lgkmcnt(0)
	v_max_i32_e32 v2, 0, v2
	v_lshl_add_u64 v[6:7], s[0:1], 0, v[2:3]
	v_lshlrev_b64 v[6:7], 11, v[6:7]
	v_lshl_add_u64 v[6:7], v[58:59], 0, v[6:7]
	global_load_dwordx2 v[124:125], v[6:7], off nt
	global_load_dwordx2 v[122:123], v[6:7], off offset:512 nt
	global_load_dwordx2 v[120:121], v[6:7], off offset:1024 nt
	global_load_dwordx2 v[118:119], v[6:7], off offset:1536 nt
.LBB0_1172:
	s_add_u32 s0, s2, -1
	s_addc_u32 s1, s3, -1
	s_and_b64 s[0:1], s[0:1], s[2:3]
	v_cmp_lt_u64_e64 s[2:3], s[10:11], 3
	v_cmp_gt_u64_e64 s[24:25], s[10:11], 2
	s_and_b64 vcc, exec, s[2:3]
	s_cbranch_vccnz .LBB0_1174
	s_cmp_eq_u64 s[0:1], 0
	s_ff1_i32_b64 s2, s[0:1]
	s_cselect_b32 s2, s14, s2
	v_or_b32_e32 v2, s2, v174
	v_lshlrev_b32_e32 v2, 2, v2
	ds_bpermute_b32 v2, v2, v166
	s_lshl_b32 s2, s2, 12
	s_add_u32 s2, s2, s34
	s_addc_u32 s3, 0, s35
	s_waitcnt lgkmcnt(0)
	v_max_i32_e32 v2, 0, v2
	v_lshl_add_u64 v[6:7], s[2:3], 0, v[2:3]
	v_lshlrev_b64 v[6:7], 11, v[6:7]
	v_lshl_add_u64 v[6:7], v[58:59], 0, v[6:7]
	global_load_dwordx2 v[116:117], v[6:7], off nt
	global_load_dwordx2 v[114:115], v[6:7], off offset:512 nt
	global_load_dwordx2 v[112:113], v[6:7], off offset:1024 nt
	global_load_dwordx2 v[110:111], v[6:7], off offset:1536 nt
; template <int R, bool RT = false>
; __device__ __forceinline__ void norm_phase(const NormArgs& a, LAS unsigned char* lds, bool ctx_rows, const float* ctx_src, const float* ctx_shift, const float* ctx_scale) {
;     ...
;                 for (int q = 0; q < R; ++q) { mask[q] = __ballot(sl[q] >= 0); cnt[q] = __builtin_popcountll(mask[q]);
; #pragma unroll
;                     for (int i = 0; i < 4; ++i) { if (mask[q]) { ee[q][i] = __builtin_ctzll(mask[q]); mask[q] &= mask[q] - 1; wgt[q][i] = 1.f; } else { ee[q][i] = i ? ee[q][0] : 0; wgt[q][i] = 0.f; } }
; #pragma unroll
;                     for (int i = 0; i < 4; ++i) {
;                         if (i < cnt[q]) { int slot = __shfl(sl[q], ee[q][i]); slot = slot < 0 ? 0 : slot; const f16* yr = a.y2 + ((size_t)ee[q][i] * EROWS + b * CAP + slot) * DM + 4 * lane;
; #pragma unroll
;                             for (int j = 0; j < 4; ++j) ld[q][i][j] = *(const f16x4*)(yr + 256 * j); } } }
.LBB0_1174:
	s_add_u32 s2, s0, -1
	s_addc_u32 s3, s1, -1
	s_and_b64 s[20:21], s[2:3], s[0:1]
	v_cmp_lt_u64_e64 s[0:1], s[10:11], 4
	v_cmp_gt_u64_e64 s[22:23], s[10:11], 3
	s_and_b64 vcc, exec, s[0:1]
	s_cbranch_vccnz .LBB0_1176
	s_cmp_eq_u64 s[20:21], 0
	s_ff1_i32_b64 s0, s[20:21]
	s_cselect_b32 s0, s14, s0
	v_or_b32_e32 v2, s0, v174
	v_lshlrev_b32_e32 v2, 2, v2
	ds_bpermute_b32 v2, v2, v166
	s_lshl_b32 s0, s0, 12
	s_add_u32 s0, s0, s34
	s_addc_u32 s1, 0, s35
	s_waitcnt lgkmcnt(0)
	v_max_i32_e32 v2, 0, v2
	v_lshl_add_u64 v[6:7], s[0:1], 0, v[2:3]
	v_lshlrev_b64 v[6:7], 11, v[6:7]
	v_lshl_add_u64 v[6:7], v[58:59], 0, v[6:7]
	global_load_dwordx2 v[108:109], v[6:7], off nt
	global_load_dwordx2 v[106:107], v[6:7], off offset:512 nt
	global_load_dwordx2 v[104:105], v[6:7], off offset:1024 nt
	global_load_dwordx2 v[102:103], v[6:7], off offset:1536 nt
.LBB0_1176:
	s_waitcnt lgkmcnt(0)
	v_cndmask_b32_e64 v183, -1, v4, s[4:5]
	v_cmp_lt_i32_e32 vcc, -1, v183
	s_cmp_eq_u64 vcc, 0
	s_cselect_b64 s[0:1], -1, 0
	s_cmp_lg_u64 vcc, 0
	s_cselect_b64 s[18:19], -1, 0
	s_ff1_i32_b64 s14, vcc
	s_cbranch_vccz .LBB0_1178
	v_or_b32_e32 v2, s14, v174
	v_lshlrev_b32_e32 v2, 2, v2
	ds_bpermute_b32 v2, v2, v183
	s_mov_b32 s15, s11
	s_lshl_b64 s[2:3], s[14:15], 12
	s_add_u32 s2, s2, s34
	s_addc_u32 s3, s3, s35
	s_waitcnt lgkmcnt(0)
	v_max_i32_e32 v2, 0, v2
	v_lshl_add_u64 v[4:5], s[2:3], 0, v[2:3]
	v_lshlrev_b64 v[4:5], 11, v[4:5]
	v_lshl_add_u64 v[4:5], v[58:59], 0, v[4:5]
	global_load_dwordx2 v[100:101], v[4:5], off nt
	global_load_dwordx2 v[98:99], v[4:5], off offset:512 nt
	global_load_dwordx2 v[96:97], v[4:5], off offset:1024 nt
	global_load_dwordx2 v[94:95], v[4:5], off offset:1536 nt
.LBB0_1178:
	s_bcnt1_i32_b64 s10, vcc
	s_add_u32 s2, vcc_lo, -1
	s_addc_u32 s3, vcc_hi, -1
	s_and_b64 s[2:3], s[2:3], vcc
	s_and_b64 s[0:1], s[0:1], exec
	v_cmp_lt_u64_e64 s[0:1], s[10:11], 2
	s_cselect_b32 s37, 0, s14
	v_cmp_gt_u64_e64 s[16:17], s[10:11], 1
	s_and_b64 vcc, exec, s[0:1]
	s_cbranch_vccnz .LBB0_1180
	s_cmp_eq_u64 s[2:3], 0
	s_ff1_i32_b64 s0, s[2:3]
	s_cselect_b32 s0, s37, s0
	v_or_b32_e32 v2, s0, v174
	v_lshlrev_b32_e32 v2, 2, v2
	ds_bpermute_b32 v2, v2, v183
	s_lshl_b32 s0, s0, 12
	s_add_u32 s0, s0, s34
	s_addc_u32 s1, 0, s35
	s_waitcnt lgkmcnt(0)
	v_max_i32_e32 v2, 0, v2
	v_lshl_add_u64 v[4:5], s[0:1], 0, v[2:3]
	v_lshlrev_b64 v[4:5], 11, v[4:5]
	v_lshl_add_u64 v[4:5], v[58:59], 0, v[4:5]
	global_load_dwordx2 v[92:93], v[4:5], off nt
	global_load_dwordx2 v[90:91], v[4:5], off offset:512 nt
	global_load_dwordx2 v[88:89], v[4:5], off offset:1024 nt
	global_load_dwordx2 v[86:87], v[4:5], off offset:1536 nt
.LBB0_1180:
	s_add_u32 s0, s2, -1
	s_addc_u32 s1, s3, -1
	s_and_b64 s[0:1], s[0:1], s[2:3]
	v_cmp_lt_u64_e64 s[2:3], s[10:11], 3
	v_cmp_gt_u64_e64 s[14:15], s[10:11], 2
	s_and_b64 vcc, exec, s[2:3]
	s_cbranch_vccnz .LBB0_1182
	s_cmp_eq_u64 s[0:1], 0
	s_ff1_i32_b64 s2, s[0:1]
	s_cselect_b32 s2, s37, s2
	v_or_b32_e32 v2, s2, v174
	v_lshlrev_b32_e32 v2, 2, v2
	ds_bpermute_b32 v2, v2, v183
	s_lshl_b32 s2, s2, 12
	s_add_u32 s2, s2, s34
	s_addc_u32 s3, 0, s35
	s_waitcnt lgkmcnt(0)
	v_max_i32_e32 v2, 0, v2
	v_lshl_add_u64 v[4:5], s[2:3], 0, v[2:3]
	v_lshlrev_b64 v[4:5], 11, v[4:5]
	v_lshl_add_u64 v[4:5], v[58:59], 0, v[4:5]
	global_load_dwordx2 v[84:85], v[4:5], off nt
	global_load_dwordx2 v[82:83], v[4:5], off offset:512 nt
	global_load_dwordx2 v[80:81], v[4:5], off offset:1024 nt
	global_load_dwordx2 v[78:79], v[4:5], off offset:1536 nt
.LBB0_1182:
	s_add_u32 s2, s0, -1
	s_addc_u32 s3, s1, -1
	v_cmp_lt_u64_e64 s[38:39], s[10:11], 4
	s_and_b64 s[0:1], s[2:3], s[0:1]
	v_cmp_gt_u64_e64 s[2:3], s[10:11], 3
	s_and_b64 vcc, exec, s[38:39]
	s_cbranch_vccnz .LBB0_1184
	s_cmp_eq_u64 s[0:1], 0
	s_ff1_i32_b64 s10, s[0:1]
	s_cselect_b32 s10, s37, s10
	v_or_b32_e32 v2, s10, v174
	v_lshlrev_b32_e32 v2, 2, v2
	ds_bpermute_b32 v2, v2, v183
	s_lshl_b32 s10, s10, 12
	s_add_u32 s38, s10, s34
	s_addc_u32 s39, 0, s35
	s_waitcnt lgkmcnt(0)
	v_max_i32_e32 v2, 0, v2
	v_lshl_add_u64 v[4:5], s[38:39], 0, v[2:3]
	v_lshlrev_b64 v[4:5], 11, v[4:5]
	v_lshl_add_u64 v[4:5], v[58:59], 0, v[4:5]
	global_load_dwordx2 v[76:77], v[4:5], off nt
	global_load_dwordx2 v[74:75], v[4:5], off offset:512 nt
	global_load_dwordx2 v[72:73], v[4:5], off offset:1024 nt
	global_load_dwordx2 v[70:71], v[4:5], off offset:1536 nt

; template <int R, bool RT = false>
; __device__ __forceinline__ void norm_phase(const NormArgs& a, LAS unsigned char* lds, bool ctx_rows, const float* ctx_src, const float* ctx_shift, const float* ctx_scale) {
;     ...
;                     while (mask[q]) {
;                         const int e2 = __builtin_ctzll(mask[q]); mask[q] &= mask[q] - 1; const int slot = __shfl(sl[q], e2); const f16* yr = a.y2 + ((size_t)e2 * EROWS + b * CAP + slot) * DM + 4 * lane;
; #pragma unroll
;                         for (int j = 0; j < 4; ++j) { const f16x4 t = *(const f16x4*)(yr + 256 * j); cs[j][0] += (float)t[0]; cs[j][1] += (float)t[1]; cs[j][2] += (float)t[2]; cs[j][3] += (float)t[3]; }
;                     }
.LBB0_1192:
	s_ff1_i32_b64 s10, s[20:21]
	v_or_b32_e32 v2, s10, v174
	v_lshlrev_b32_e32 v2, 2, v2
	ds_bpermute_b32 v168, v2, v166
	s_add_u32 s22, s20, -1
	s_addc_u32 s23, s21, -1
	s_lshl_b32 s10, s10, 12
	s_add_u32 s24, s10, s34
	s_addc_u32 s25, 0, s35
	s_waitcnt lgkmcnt(0)
	v_ashrrev_i32_e32 v169, 31, v168
	v_lshl_add_u64 v[168:169], s[24:25], 0, v[168:169]
	v_lshlrev_b64 v[168:169], 11, v[168:169]
	v_lshl_add_u64 v[168:169], v[58:59], 0, v[168:169]
	global_load_dwordx2 v[170:171], v[168:169], off nt
	global_load_dwordx2 v[172:173], v[168:169], off offset:512 nt
	global_load_dwordx2 v[184:185], v[168:169], off offset:1024 nt
	s_nop 0
	global_load_dwordx2 v[168:169], v[168:169], off offset:1536 nt
	s_and_b64 s[20:21], s[22:23], s[20:21]
	s_cmp_lg_u64 s[20:21], 0
	s_waitcnt vmcnt(3)
	v_cvt_f32_f16_e32 v186, v170
	v_cvt_f32_f16_sdwa v187, v170 dst_sel:DWORD dst_unused:UNUSED_PAD src0_sel:WORD_1
	v_cvt_f32_f16_e32 v170, v171
	v_cvt_f32_f16_sdwa v171, v171 dst_sel:DWORD dst_unused:UNUSED_PAD src0_sel:WORD_1
	s_waitcnt vmcnt(2)
	v_cvt_f32_f16_e32 v188, v172
	v_cvt_f32_f16_sdwa v189, v172 dst_sel:DWORD dst_unused:UNUSED_PAD src0_sel:WORD_1
	v_cvt_f32_f16_e32 v172, v173
	v_cvt_f32_f16_sdwa v173, v173 dst_sel:DWORD dst_unused:UNUSED_PAD src0_sel:WORD_1
	s_waitcnt vmcnt(1)
	v_cvt_f32_f16_e32 v190, v184
	v_cvt_f32_f16_e32 v192, v185
	s_waitcnt vmcnt(0)
	v_cvt_f32_f16_e32 v194, v168
	v_cvt_f32_f16_e32 v196, v169
	v_cvt_f32_f16_sdwa v197, v169 dst_sel:DWORD dst_unused:UNUSED_PAD src0_sel:WORD_1
	v_cvt_f32_f16_sdwa v195, v168 dst_sel:DWORD dst_unused:UNUSED_PAD src0_sel:WORD_1
	v_cvt_f32_f16_sdwa v193, v185 dst_sel:DWORD dst_unused:UNUSED_PAD src0_sel:WORD_1
	v_cvt_f32_f16_sdwa v191, v184 dst_sel:DWORD dst_unused:UNUSED_PAD src0_sel:WORD_1
	v_pk_add_f32 v[18:19], v[18:19], v[196:197]
	v_pk_add_f32 v[16:17], v[16:17], v[194:195]
	v_pk_add_f32 v[14:15], v[14:15], v[192:193]
	v_pk_add_f32 v[12:13], v[12:13], v[190:191]
	v_pk_add_f32 v[10:11], v[10:11], v[172:173]
	v_pk_add_f32 v[8:9], v[8:9], v[188:189]
	v_pk_add_f32 v[6:7], v[6:7], v[170:171]
	v_pk_add_f32 v[4:5], v[4:5], v[186:187]
	s_cbranch_scc1 .LBB0_1192

; template <int R, bool RT = false>
; __device__ __forceinline__ void norm_phase(const NormArgs& a, LAS unsigned char* lds, bool ctx_rows, const float* ctx_src, const float* ctx_shift, const float* ctx_scale) {
;     ...
;                     while (mask[q]) {
;                         const int e2 = __builtin_ctzll(mask[q]); mask[q] &= mask[q] - 1; const int slot = __shfl(sl[q], e2); const f16* yr = a.y2 + ((size_t)e2 * EROWS + b * CAP + slot) * DM + 4 * lane;
; #pragma unroll
;                         for (int j = 0; j < 4; ++j) { const f16x4 t = *(const f16x4*)(yr + 256 * j); cs[j][0] += (float)t[0]; cs[j][1] += (float)t[1]; cs[j][2] += (float)t[2]; cs[j][3] += (float)t[3]; }
.LBB0_1202:
	s_ff1_i32_b64 s10, s[0:1]
	v_or_b32_e32 v2, s10, v174
	v_lshlrev_b32_e32 v2, 2, v2
	ds_bpermute_b32 v184, v2, v183
	s_add_u32 s2, s0, -1
	s_addc_u32 s3, s1, -1
	s_lshl_b32 s10, s10, 12
	s_add_u32 s14, s10, s34
	s_addc_u32 s15, 0, s35
	s_waitcnt lgkmcnt(0)
	v_ashrrev_i32_e32 v185, 31, v184
	v_lshl_add_u64 v[184:185], s[14:15], 0, v[184:185]
	v_lshlrev_b64 v[184:185], 11, v[184:185]
	v_lshl_add_u64 v[184:185], v[58:59], 0, v[184:185]
	global_load_dwordx2 v[186:187], v[184:185], off nt
	global_load_dwordx2 v[188:189], v[184:185], off offset:512 nt
	global_load_dwordx2 v[190:191], v[184:185], off offset:1024 nt
	s_nop 0
	global_load_dwordx2 v[184:185], v[184:185], off offset:1536 nt
	s_and_b64 s[0:1], s[2:3], s[0:1]
	s_cmp_lg_u64 s[0:1], 0
	s_waitcnt vmcnt(3)
	v_cvt_f32_f16_e32 v192, v186
	v_cvt_f32_f16_sdwa v193, v186 dst_sel:DWORD dst_unused:UNUSED_PAD src0_sel:WORD_1
	v_cvt_f32_f16_e32 v186, v187
	v_cvt_f32_f16_sdwa v187, v187 dst_sel:DWORD dst_unused:UNUSED_PAD src0_sel:WORD_1
	s_waitcnt vmcnt(2)
	v_cvt_f32_f16_e32 v194, v188
	v_cvt_f32_f16_sdwa v195, v188 dst_sel:DWORD dst_unused:UNUSED_PAD src0_sel:WORD_1
	v_cvt_f32_f16_e32 v188, v189
	v_cvt_f32_f16_sdwa v189, v189 dst_sel:DWORD dst_unused:UNUSED_PAD src0_sel:WORD_1
	s_waitcnt vmcnt(1)
	v_cvt_f32_f16_e32 v196, v190
	v_cvt_f32_f16_e32 v198, v191
	s_waitcnt vmcnt(0)
	v_cvt_f32_f16_e32 v200, v184
	v_cvt_f32_f16_e32 v202, v185
	v_cvt_f32_f16_sdwa v203, v185 dst_sel:DWORD dst_unused:UNUSED_PAD src0_sel:WORD_1
	v_cvt_f32_f16_sdwa v201, v184 dst_sel:DWORD dst_unused:UNUSED_PAD src0_sel:WORD_1
	v_cvt_f32_f16_sdwa v199, v191 dst_sel:DWORD dst_unused:UNUSED_PAD src0_sel:WORD_1
	v_cvt_f32_f16_sdwa v197, v190 dst_sel:DWORD dst_unused:UNUSED_PAD src0_sel:WORD_1
	v_pk_add_f32 v[18:19], v[18:19], v[202:203]
	v_pk_add_f32 v[16:17], v[16:17], v[200:201]
	v_pk_add_f32 v[14:15], v[14:15], v[198:199]
	v_pk_add_f32 v[12:13], v[12:13], v[196:197]
	v_pk_add_f32 v[10:11], v[10:11], v[188:189]
	v_pk_add_f32 v[8:9], v[8:9], v[194:195]
	v_pk_add_f32 v[6:7], v[6:7], v[186:187]
	v_pk_add_f32 v[4:5], v[4:5], v[192:193]
	s_cbranch_scc1 .LBB0_1202
